# loop-edge: G1/G2 K-loop counter/pointer SALU block moved in front of the loop-back barrier (same bytes, reordered)
# speedup vs baseline: 1.0007x; 1.0002x over previous
.LBB0_310:
	v_add_u32_e32 v64, s34, v185
	ds_read_b128 v[130:133], v64
	ds_read_b128 v[134:137], v64 offset:1024
	ds_read_b128 v[138:141], v64 offset:2048
	ds_read_b128 v[142:145], v64 offset:3072
	v_add_u32_e32 v64, s37, v185
	ds_read_b128 v[158:161], v64
	ds_read_b128 v[162:165], v64 offset:1024
	ds_read_b128 v[166:169], v64 offset:2048
	ds_read_b128 v[170:173], v64 offset:3072
	s_add_u32 s26, s24, 0xfffc0080
	s_addc_u32 s27, s25, -1
	s_cmp_eq_u32 s56, 12
	s_cselect_b32 s29, s19, s27
	s_cselect_b32 s28, s33, s26
	s_cselect_b32 s27, s17, s55
	s_cselect_b32 s26, s53, s54
	s_add_i32 m0, s40, 0xc000
	ds_read_b128 v[174:177], v188
	ds_read_b128 v[178:181], v188 offset:1024
	ds_read_b128 v[190:193], v188 offset:2048
	ds_read_b128 v[212:215], v188 offset:3072
	ds_read_b128 v[216:219], v188 offset:4096
	ds_read_b128 v[220:223], v188 offset:5120
	ds_read_b128 v[224:227], v188 offset:6144
	ds_read_b128 v[228:231], v188 offset:7168
	global_load_lds_dwordx4 v154, s[24:25]
	s_add_i32 m0, s40, 0xe000
	s_nop 0
	global_load_lds_dwordx4 v156, s[24:25]
	s_waitcnt vmcnt(8)
	s_waitcnt lgkmcnt(0)
	s_barrier
	s_setprio 1
	s_waitcnt lgkmcnt(0)
	v_mfma_f32_16x16x32_bf16 v[126:129], v[130:133], v[174:177], v[126:129]
	v_mfma_f32_16x16x32_bf16 v[122:125], v[138:141], v[174:177], v[122:125]
	v_mfma_f32_16x16x32_bf16 v[118:121], v[130:133], v[190:193], v[118:121]
	v_mfma_f32_16x16x32_bf16 v[110:113], v[138:141], v[190:193], v[110:113]
	v_mfma_f32_16x16x32_bf16 v[102:105], v[130:133], v[216:219], v[102:105]
	v_mfma_f32_16x16x32_bf16 v[94:97], v[138:141], v[216:219], v[94:97]
	v_mfma_f32_16x16x32_bf16 v[86:89], v[130:133], v[224:227], v[86:89]
	v_mfma_f32_16x16x32_bf16 v[78:81], v[138:141], v[224:227], v[78:81]
	v_mfma_f32_16x16x32_bf16 v[126:129], v[134:137], v[178:181], v[126:129]
	v_mfma_f32_16x16x32_bf16 v[122:125], v[142:145], v[178:181], v[122:125]
	v_mfma_f32_16x16x32_bf16 v[118:121], v[134:137], v[212:215], v[118:121]
	v_mfma_f32_16x16x32_bf16 v[110:113], v[142:145], v[212:215], v[110:113]
	v_mfma_f32_16x16x32_bf16 v[102:105], v[134:137], v[220:223], v[102:105]
	v_mfma_f32_16x16x32_bf16 v[94:97], v[142:145], v[220:223], v[94:97]
	v_mfma_f32_16x16x32_bf16 v[86:89], v[134:137], v[228:231], v[86:89]
	v_mfma_f32_16x16x32_bf16 v[78:81], v[142:145], v[228:231], v[78:81]
	s_setprio 0
	s_setprio 1
	v_mfma_f32_16x16x32_bf16 v[114:117], v[158:161], v[174:177], v[114:117]
	v_mfma_f32_16x16x32_bf16 v[106:109], v[166:169], v[174:177], v[106:109]
	v_mfma_f32_16x16x32_bf16 v[98:101], v[158:161], v[190:193], v[98:101]
	v_mfma_f32_16x16x32_bf16 v[90:93], v[166:169], v[190:193], v[90:93]
	v_mfma_f32_16x16x32_bf16 v[82:85], v[158:161], v[216:219], v[82:85]
	v_mfma_f32_16x16x32_bf16 v[74:77], v[166:169], v[216:219], v[74:77]
	v_mfma_f32_16x16x32_bf16 v[70:73], v[158:161], v[224:227], v[70:73]
	v_mfma_f32_16x16x32_bf16 v[66:69], v[166:169], v[224:227], v[66:69]
	v_mfma_f32_16x16x32_bf16 v[114:117], v[162:165], v[178:181], v[114:117]
	v_mfma_f32_16x16x32_bf16 v[106:109], v[170:173], v[178:181], v[106:109]
	v_mfma_f32_16x16x32_bf16 v[98:101], v[162:165], v[212:215], v[98:101]
	v_mfma_f32_16x16x32_bf16 v[90:93], v[170:173], v[212:215], v[90:93]
	v_mfma_f32_16x16x32_bf16 v[82:85], v[162:165], v[220:223], v[82:85]
	v_mfma_f32_16x16x32_bf16 v[74:77], v[170:173], v[220:223], v[74:77]
	v_mfma_f32_16x16x32_bf16 v[70:73], v[162:165], v[228:231], v[70:73]
	v_mfma_f32_16x16x32_bf16 v[66:69], v[170:173], v[228:231], v[66:69]
	s_setprio 0
	s_barrier
	s_mov_b32 m0, s35
	s_add_u32 s58, s26, 0x40000
	ds_read_b128 v[174:177], v188 offset:16384
	ds_read_b128 v[178:181], v188 offset:17408
	ds_read_b128 v[190:193], v188 offset:18432
	ds_read_b128 v[212:215], v188 offset:19456
	ds_read_b128 v[216:219], v188 offset:20480
	ds_read_b128 v[220:223], v188 offset:21504
	ds_read_b128 v[224:227], v188 offset:22528
	ds_read_b128 v[228:231], v188 offset:23552
	global_load_lds_dwordx4 v150, s[26:27]
	s_mov_b32 m0, s36
	s_addc_u32 s59, s27, 0
	global_load_lds_dwordx4 v146, s[26:27]
	s_mov_b32 m0, s38
	s_nop 0
	global_load_lds_dwordx4 v150, s[58:59]
	s_mov_b32 m0, s39
	s_nop 0
	global_load_lds_dwordx4 v146, s[58:59]
	s_mov_b32 m0, s40
	s_nop 0
	global_load_lds_dwordx4 v152, s[28:29]
	s_mov_b32 m0, s41
	s_nop 0
	global_load_lds_dwordx4 v148, s[28:29]
	s_waitcnt vmcnt(8)
	s_waitcnt lgkmcnt(0)
	s_barrier
	s_setprio 1
	s_waitcnt lgkmcnt(0)
	v_mfma_f32_16x16x32_bf16 v[60:63], v[130:133], v[174:177], v[60:63]
	v_mfma_f32_16x16x32_bf16 v[56:59], v[138:141], v[174:177], v[56:59]
	v_mfma_f32_16x16x32_bf16 v[52:55], v[130:133], v[190:193], v[52:55]
	v_mfma_f32_16x16x32_bf16 v[44:47], v[138:141], v[190:193], v[44:47]
	v_mfma_f32_16x16x32_bf16 v[36:39], v[130:133], v[216:219], v[36:39]
	v_mfma_f32_16x16x32_bf16 v[28:31], v[138:141], v[216:219], v[28:31]
	v_mfma_f32_16x16x32_bf16 v[20:23], v[130:133], v[224:227], v[20:23]
	v_mfma_f32_16x16x32_bf16 v[12:15], v[138:141], v[224:227], v[12:15]
	v_mfma_f32_16x16x32_bf16 v[60:63], v[134:137], v[178:181], v[60:63]
	v_mfma_f32_16x16x32_bf16 v[56:59], v[142:145], v[178:181], v[56:59]
	v_mfma_f32_16x16x32_bf16 v[52:55], v[134:137], v[212:215], v[52:55]
	v_mfma_f32_16x16x32_bf16 v[44:47], v[142:145], v[212:215], v[44:47]
	v_mfma_f32_16x16x32_bf16 v[36:39], v[134:137], v[220:223], v[36:39]
	v_mfma_f32_16x16x32_bf16 v[28:31], v[142:145], v[220:223], v[28:31]
	v_mfma_f32_16x16x32_bf16 v[20:23], v[134:137], v[228:231], v[20:23]
	v_mfma_f32_16x16x32_bf16 v[12:15], v[142:145], v[228:231], v[12:15]
	s_setprio 0
	s_setprio 1
	v_mfma_f32_16x16x32_bf16 v[48:51], v[158:161], v[174:177], v[48:51]
	v_mfma_f32_16x16x32_bf16 v[40:43], v[166:169], v[174:177], v[40:43]
	v_mfma_f32_16x16x32_bf16 v[32:35], v[158:161], v[190:193], v[32:35]
	v_mfma_f32_16x16x32_bf16 v[24:27], v[166:169], v[190:193], v[24:27]
	v_mfma_f32_16x16x32_bf16 v[16:19], v[158:161], v[216:219], v[16:19]
	v_mfma_f32_16x16x32_bf16 v[8:11], v[166:169], v[216:219], v[8:11]
	v_mfma_f32_16x16x32_bf16 v[4:7], v[158:161], v[224:227], v[4:7]
	v_mfma_f32_16x16x32_bf16 v[0:3], v[166:169], v[224:227], v[0:3]
	v_mfma_f32_16x16x32_bf16 v[48:51], v[162:165], v[178:181], v[48:51]
	v_mfma_f32_16x16x32_bf16 v[40:43], v[170:173], v[178:181], v[40:43]
	v_mfma_f32_16x16x32_bf16 v[32:35], v[162:165], v[212:215], v[32:35]
	v_mfma_f32_16x16x32_bf16 v[24:27], v[170:173], v[212:215], v[24:27]
	v_mfma_f32_16x16x32_bf16 v[16:19], v[162:165], v[220:223], v[16:19]
	v_mfma_f32_16x16x32_bf16 v[8:11], v[170:173], v[220:223], v[8:11]
	v_mfma_f32_16x16x32_bf16 v[4:7], v[162:165], v[228:231], v[4:7]
	v_mfma_f32_16x16x32_bf16 v[0:3], v[170:173], v[228:231], v[0:3]
	s_setprio 0
	s_barrier
	v_add_u32_e32 v64, s44, v185
	ds_read_b128 v[130:133], v64
	ds_read_b128 v[134:137], v64 offset:1024
	ds_read_b128 v[138:141], v64 offset:2048
	ds_read_b128 v[142:145], v64 offset:3072
	v_add_u32_e32 v64, s49, v185
	ds_read_b128 v[158:161], v64
	ds_read_b128 v[162:165], v64 offset:1024
	ds_read_b128 v[166:169], v64 offset:2048
	ds_read_b128 v[170:173], v64 offset:3072
	s_add_u32 s28, s28, 0x40000
	s_addc_u32 s29, s29, 0
	s_mov_b32 m0, s42
	ds_read_b128 v[174:177], v188 offset:32768
	ds_read_b128 v[178:181], v188 offset:33792
	ds_read_b128 v[190:193], v188 offset:34816
	ds_read_b128 v[212:215], v188 offset:35840
	ds_read_b128 v[216:219], v188 offset:36864
	ds_read_b128 v[220:223], v188 offset:37888
	ds_read_b128 v[224:227], v188 offset:38912
	ds_read_b128 v[228:231], v188 offset:39936
	global_load_lds_dwordx4 v152, s[28:29]
	s_mov_b32 m0, s43
	s_nop 0
	global_load_lds_dwordx4 v148, s[28:29]
	s_waitcnt vmcnt(8)
	s_waitcnt lgkmcnt(0)
	s_barrier
	s_setprio 1
	s_waitcnt lgkmcnt(0)
	v_mfma_f32_16x16x32_bf16 v[126:129], v[130:133], v[174:177], v[126:129]
	v_mfma_f32_16x16x32_bf16 v[122:125], v[138:141], v[174:177], v[122:125]
	v_mfma_f32_16x16x32_bf16 v[118:121], v[130:133], v[190:193], v[118:121]
	v_mfma_f32_16x16x32_bf16 v[110:113], v[138:141], v[190:193], v[110:113]
	v_mfma_f32_16x16x32_bf16 v[102:105], v[130:133], v[216:219], v[102:105]
	v_mfma_f32_16x16x32_bf16 v[94:97], v[138:141], v[216:219], v[94:97]
	v_mfma_f32_16x16x32_bf16 v[86:89], v[130:133], v[224:227], v[86:89]
	v_mfma_f32_16x16x32_bf16 v[78:81], v[138:141], v[224:227], v[78:81]
	v_mfma_f32_16x16x32_bf16 v[126:129], v[134:137], v[178:181], v[126:129]
	v_mfma_f32_16x16x32_bf16 v[122:125], v[142:145], v[178:181], v[122:125]
	v_mfma_f32_16x16x32_bf16 v[118:121], v[134:137], v[212:215], v[118:121]
	v_mfma_f32_16x16x32_bf16 v[110:113], v[142:145], v[212:215], v[110:113]
	v_mfma_f32_16x16x32_bf16 v[102:105], v[134:137], v[220:223], v[102:105]
	v_mfma_f32_16x16x32_bf16 v[94:97], v[142:145], v[220:223], v[94:97]
	v_mfma_f32_16x16x32_bf16 v[86:89], v[134:137], v[228:231], v[86:89]
	v_mfma_f32_16x16x32_bf16 v[78:81], v[142:145], v[228:231], v[78:81]
	s_setprio 0
	s_setprio 1
	v_mfma_f32_16x16x32_bf16 v[114:117], v[158:161], v[174:177], v[114:117]
	v_mfma_f32_16x16x32_bf16 v[106:109], v[166:169], v[174:177], v[106:109]
	v_mfma_f32_16x16x32_bf16 v[98:101], v[158:161], v[190:193], v[98:101]
	v_mfma_f32_16x16x32_bf16 v[90:93], v[166:169], v[190:193], v[90:93]
	v_mfma_f32_16x16x32_bf16 v[82:85], v[158:161], v[216:219], v[82:85]
	v_mfma_f32_16x16x32_bf16 v[74:77], v[166:169], v[216:219], v[74:77]
	v_mfma_f32_16x16x32_bf16 v[70:73], v[158:161], v[224:227], v[70:73]
	v_mfma_f32_16x16x32_bf16 v[66:69], v[166:169], v[224:227], v[66:69]
	v_mfma_f32_16x16x32_bf16 v[114:117], v[162:165], v[178:181], v[114:117]
	v_mfma_f32_16x16x32_bf16 v[106:109], v[170:173], v[178:181], v[106:109]
	v_mfma_f32_16x16x32_bf16 v[98:101], v[162:165], v[212:215], v[98:101]
	v_mfma_f32_16x16x32_bf16 v[90:93], v[170:173], v[212:215], v[90:93]
	v_mfma_f32_16x16x32_bf16 v[82:85], v[162:165], v[220:223], v[82:85]
	v_mfma_f32_16x16x32_bf16 v[74:77], v[170:173], v[220:223], v[74:77]
	v_mfma_f32_16x16x32_bf16 v[70:73], v[162:165], v[228:231], v[70:73]
	v_mfma_f32_16x16x32_bf16 v[66:69], v[170:173], v[228:231], v[66:69]
	s_setprio 0
	s_barrier
	s_mov_b32 m0, s45
	s_add_u32 s100, s26, s68
	s_addc_u32 s101, s27, s69
	s_add_u32 s26, s26, 0x40080
	ds_read_b128 v[174:177], v188 offset:49152
	ds_read_b128 v[178:181], v188 offset:50176
	ds_read_b128 v[190:193], v188 offset:51200
	ds_read_b128 v[212:215], v188 offset:52224
	ds_read_b128 v[216:219], v188 offset:53248
	ds_read_b128 v[220:223], v188 offset:54272
	ds_read_b128 v[224:227], v188 offset:55296
	ds_read_b128 v[228:231], v188 offset:56320
	global_load_lds_dwordx4 v150, s[100:101]
	s_mov_b32 m0, s46
	s_addc_u32 s27, s27, 0
	global_load_lds_dwordx4 v146, s[100:101]
	s_mov_b32 m0, s50
	s_add_u32 s100, s28, s68
	global_load_lds_dwordx4 v150, s[26:27]
	s_addc_u32 s101, s29, s69
	s_mov_b32 m0, s51
	s_sub_u32 s100, s100, 0x40000
	global_load_lds_dwordx4 v146, s[26:27]
	s_subb_u32 s101, s101, 0
	s_mov_b32 m0, s47
	s_nop 0
	global_load_lds_dwordx4 v152, s[100:101]
	s_mov_b32 m0, s48
	s_nop 0
	global_load_lds_dwordx4 v148, s[100:101]
	s_waitcnt vmcnt(8)
	s_waitcnt lgkmcnt(0)
	s_barrier
	s_setprio 1
	s_waitcnt lgkmcnt(0)
	v_mfma_f32_16x16x32_bf16 v[60:63], v[130:133], v[174:177], v[60:63]
	v_mfma_f32_16x16x32_bf16 v[56:59], v[138:141], v[174:177], v[56:59]
	v_mfma_f32_16x16x32_bf16 v[52:55], v[130:133], v[190:193], v[52:55]
	v_mfma_f32_16x16x32_bf16 v[44:47], v[138:141], v[190:193], v[44:47]
	v_mfma_f32_16x16x32_bf16 v[36:39], v[130:133], v[216:219], v[36:39]
	v_mfma_f32_16x16x32_bf16 v[28:31], v[138:141], v[216:219], v[28:31]
	v_mfma_f32_16x16x32_bf16 v[20:23], v[130:133], v[224:227], v[20:23]
	v_mfma_f32_16x16x32_bf16 v[12:15], v[138:141], v[224:227], v[12:15]
	v_mfma_f32_16x16x32_bf16 v[60:63], v[134:137], v[178:181], v[60:63]
	v_mfma_f32_16x16x32_bf16 v[56:59], v[142:145], v[178:181], v[56:59]
	v_mfma_f32_16x16x32_bf16 v[52:55], v[134:137], v[212:215], v[52:55]
	v_mfma_f32_16x16x32_bf16 v[44:47], v[142:145], v[212:215], v[44:47]
	v_mfma_f32_16x16x32_bf16 v[36:39], v[134:137], v[220:223], v[36:39]
	v_mfma_f32_16x16x32_bf16 v[28:31], v[142:145], v[220:223], v[28:31]
	v_mfma_f32_16x16x32_bf16 v[20:23], v[134:137], v[228:231], v[20:23]
	v_mfma_f32_16x16x32_bf16 v[12:15], v[142:145], v[228:231], v[12:15]
	s_setprio 0
	s_setprio 1
	v_mfma_f32_16x16x32_bf16 v[48:51], v[158:161], v[174:177], v[48:51]
	v_mfma_f32_16x16x32_bf16 v[40:43], v[166:169], v[174:177], v[40:43]
	v_mfma_f32_16x16x32_bf16 v[32:35], v[158:161], v[190:193], v[32:35]
	v_mfma_f32_16x16x32_bf16 v[24:27], v[166:169], v[190:193], v[24:27]
	v_mfma_f32_16x16x32_bf16 v[16:19], v[158:161], v[216:219], v[16:19]
	v_mfma_f32_16x16x32_bf16 v[8:11], v[166:169], v[216:219], v[8:11]
	v_mfma_f32_16x16x32_bf16 v[4:7], v[158:161], v[224:227], v[4:7]
	v_mfma_f32_16x16x32_bf16 v[0:3], v[166:169], v[224:227], v[0:3]
	v_mfma_f32_16x16x32_bf16 v[48:51], v[162:165], v[178:181], v[48:51]
	v_mfma_f32_16x16x32_bf16 v[40:43], v[170:173], v[178:181], v[40:43]
	v_mfma_f32_16x16x32_bf16 v[32:35], v[162:165], v[212:215], v[32:35]
	v_mfma_f32_16x16x32_bf16 v[24:27], v[170:173], v[212:215], v[24:27]
	v_mfma_f32_16x16x32_bf16 v[16:19], v[162:165], v[220:223], v[16:19]
	v_mfma_f32_16x16x32_bf16 v[8:11], v[170:173], v[220:223], v[8:11]
	v_mfma_f32_16x16x32_bf16 v[4:7], v[162:165], v[228:231], v[4:7]
	v_mfma_f32_16x16x32_bf16 v[0:3], v[170:173], v[228:231], v[0:3]
	s_add_i32 s56, s56, 2
	s_add_u32 s24, s24, 0x100
	s_addc_u32 s25, s25, 0
	s_add_u32 s54, s54, 0x100
	s_addc_u32 s55, s55, 0
	s_cmp_gt_u32 s56, 13
	s_setprio 0
	s_barrier
	s_cbranch_scc0 .LBB0_310
	s_and_b64 vcc, exec, s[14:15]
	s_cbranch_vccz .LBB0_313
	s_barrier

.LBB0_814:
	v_add_u32_e32 v64, s11, v173
	ds_read_b128 v[66:69], v64
	ds_read_b128 v[70:73], v64 offset:1024
	ds_read_b128 v[74:77], v64 offset:2048
	ds_read_b128 v[78:81], v64 offset:3072
	v_add_u32_e32 v64, s34, v173
	ds_read_b128 v[146:149], v64
	ds_read_b128 v[150:153], v64 offset:1024
	ds_read_b128 v[166:169], v64 offset:2048
	ds_read_b128 v[176:179], v64 offset:3072
	s_add_u32 s4, s0, 0xfffc0080
	s_addc_u32 s5, s1, -1
	s_cmp_eq_u32 s61, 12
	s_cselect_b32 s27, s55, s5
	s_cselect_b32 s26, s56, s4
	s_cselect_b32 s5, s57, s60
	s_cselect_b32 s4, s58, s59
	s_add_i32 m0, s37, 0xc000
	ds_read_b128 v[180:183], v175
	ds_read_b128 v[184:187], v175 offset:1024
	ds_read_b128 v[188:191], v175 offset:2048
	ds_read_b128 v[192:195], v175 offset:3072
	ds_read_b128 v[212:215], v175 offset:4096
	ds_read_b128 v[216:219], v175 offset:5120
	ds_read_b128 v[220:223], v175 offset:6144
	ds_read_b128 v[224:227], v175 offset:7168
	global_load_lds_dwordx4 v162, s[0:1]
	s_add_i32 m0, s37, 0xe000
	s_nop 0
	global_load_lds_dwordx4 v164, s[0:1]
	s_waitcnt vmcnt(8)
	s_waitcnt lgkmcnt(0)
	s_barrier
	s_setprio 1
	s_waitcnt lgkmcnt(0)
	v_mfma_f32_16x16x32_bf16 v[142:145], v[66:69], v[180:183], v[142:145]
	v_mfma_f32_16x16x32_bf16 v[138:141], v[74:77], v[180:183], v[138:141]
	v_mfma_f32_16x16x32_bf16 v[126:129], v[66:69], v[188:191], v[126:129]
	v_mfma_f32_16x16x32_bf16 v[122:125], v[74:77], v[188:191], v[122:125]
	v_mfma_f32_16x16x32_bf16 v[110:113], v[66:69], v[212:215], v[110:113]
	v_mfma_f32_16x16x32_bf16 v[106:109], v[74:77], v[212:215], v[106:109]
	v_mfma_f32_16x16x32_bf16 v[94:97], v[66:69], v[220:223], v[94:97]
	v_mfma_f32_16x16x32_bf16 v[90:93], v[74:77], v[220:223], v[90:93]
	v_mfma_f32_16x16x32_bf16 v[142:145], v[70:73], v[184:187], v[142:145]
	v_mfma_f32_16x16x32_bf16 v[138:141], v[78:81], v[184:187], v[138:141]
	v_mfma_f32_16x16x32_bf16 v[126:129], v[70:73], v[192:195], v[126:129]
	v_mfma_f32_16x16x32_bf16 v[122:125], v[78:81], v[192:195], v[122:125]
	v_mfma_f32_16x16x32_bf16 v[110:113], v[70:73], v[216:219], v[110:113]
	v_mfma_f32_16x16x32_bf16 v[106:109], v[78:81], v[216:219], v[106:109]
	v_mfma_f32_16x16x32_bf16 v[94:97], v[70:73], v[224:227], v[94:97]
	v_mfma_f32_16x16x32_bf16 v[90:93], v[78:81], v[224:227], v[90:93]
	s_setprio 0
	s_setprio 1
	v_mfma_f32_16x16x32_bf16 v[134:137], v[146:149], v[180:183], v[134:137]
	v_mfma_f32_16x16x32_bf16 v[130:133], v[166:169], v[180:183], v[130:133]
	v_mfma_f32_16x16x32_bf16 v[118:121], v[146:149], v[188:191], v[118:121]
	v_mfma_f32_16x16x32_bf16 v[114:117], v[166:169], v[188:191], v[114:117]
	v_mfma_f32_16x16x32_bf16 v[102:105], v[146:149], v[212:215], v[102:105]
	v_mfma_f32_16x16x32_bf16 v[98:101], v[166:169], v[212:215], v[98:101]
	v_mfma_f32_16x16x32_bf16 v[86:89], v[146:149], v[220:223], v[86:89]
	v_mfma_f32_16x16x32_bf16 v[82:85], v[166:169], v[220:223], v[82:85]
	v_mfma_f32_16x16x32_bf16 v[134:137], v[150:153], v[184:187], v[134:137]
	v_mfma_f32_16x16x32_bf16 v[130:133], v[176:179], v[184:187], v[130:133]
	v_mfma_f32_16x16x32_bf16 v[118:121], v[150:153], v[192:195], v[118:121]
	v_mfma_f32_16x16x32_bf16 v[114:117], v[176:179], v[192:195], v[114:117]
	v_mfma_f32_16x16x32_bf16 v[102:105], v[150:153], v[216:219], v[102:105]
	v_mfma_f32_16x16x32_bf16 v[98:101], v[176:179], v[216:219], v[98:101]
	v_mfma_f32_16x16x32_bf16 v[86:89], v[150:153], v[224:227], v[86:89]
	v_mfma_f32_16x16x32_bf16 v[82:85], v[176:179], v[224:227], v[82:85]
	s_setprio 0
	s_barrier
	s_mov_b32 m0, s31
	s_add_u32 s62, s4, 0x40000
	ds_read_b128 v[180:183], v175 offset:16384
	ds_read_b128 v[184:187], v175 offset:17408
	ds_read_b128 v[188:191], v175 offset:18432
	ds_read_b128 v[192:195], v175 offset:19456
	ds_read_b128 v[212:215], v175 offset:20480
	ds_read_b128 v[216:219], v175 offset:21504
	ds_read_b128 v[220:223], v175 offset:22528
	ds_read_b128 v[224:227], v175 offset:23552
	global_load_lds_dwordx4 v158, s[4:5]
	s_mov_b32 m0, s33
	s_addc_u32 s63, s5, 0
	global_load_lds_dwordx4 v154, s[4:5]
	s_mov_b32 m0, s35
	s_nop 0
	global_load_lds_dwordx4 v158, s[62:63]
	s_mov_b32 m0, s36
	s_nop 0
	global_load_lds_dwordx4 v154, s[62:63]
	s_mov_b32 m0, s37
	s_nop 0
	global_load_lds_dwordx4 v160, s[26:27]
	s_mov_b32 m0, s38
	s_nop 0
	global_load_lds_dwordx4 v156, s[26:27]
	s_waitcnt vmcnt(8)
	s_waitcnt lgkmcnt(0)
	s_barrier
	s_setprio 1
	s_waitcnt lgkmcnt(0)
	v_mfma_f32_16x16x32_bf16 v[60:63], v[66:69], v[180:183], v[60:63]
	v_mfma_f32_16x16x32_bf16 v[56:59], v[74:77], v[180:183], v[56:59]
	v_mfma_f32_16x16x32_bf16 v[44:47], v[66:69], v[188:191], v[44:47]
	v_mfma_f32_16x16x32_bf16 v[40:43], v[74:77], v[188:191], v[40:43]
	v_mfma_f32_16x16x32_bf16 v[28:31], v[66:69], v[212:215], v[28:31]
	v_mfma_f32_16x16x32_bf16 v[24:27], v[74:77], v[212:215], v[24:27]
	v_mfma_f32_16x16x32_bf16 v[12:15], v[66:69], v[220:223], v[12:15]
	v_mfma_f32_16x16x32_bf16 v[8:11], v[74:77], v[220:223], v[8:11]
	v_mfma_f32_16x16x32_bf16 v[60:63], v[70:73], v[184:187], v[60:63]
	v_mfma_f32_16x16x32_bf16 v[56:59], v[78:81], v[184:187], v[56:59]
	v_mfma_f32_16x16x32_bf16 v[44:47], v[70:73], v[192:195], v[44:47]
	v_mfma_f32_16x16x32_bf16 v[40:43], v[78:81], v[192:195], v[40:43]
	v_mfma_f32_16x16x32_bf16 v[28:31], v[70:73], v[216:219], v[28:31]
	v_mfma_f32_16x16x32_bf16 v[24:27], v[78:81], v[216:219], v[24:27]
	v_mfma_f32_16x16x32_bf16 v[12:15], v[70:73], v[224:227], v[12:15]
	v_mfma_f32_16x16x32_bf16 v[8:11], v[78:81], v[224:227], v[8:11]
	s_setprio 0
	s_setprio 1
	v_mfma_f32_16x16x32_bf16 v[52:55], v[146:149], v[180:183], v[52:55]
	v_mfma_f32_16x16x32_bf16 v[48:51], v[166:169], v[180:183], v[48:51]
	v_mfma_f32_16x16x32_bf16 v[36:39], v[146:149], v[188:191], v[36:39]
	v_mfma_f32_16x16x32_bf16 v[32:35], v[166:169], v[188:191], v[32:35]
	v_mfma_f32_16x16x32_bf16 v[20:23], v[146:149], v[212:215], v[20:23]
	v_mfma_f32_16x16x32_bf16 v[16:19], v[166:169], v[212:215], v[16:19]
	v_mfma_f32_16x16x32_bf16 v[4:7], v[146:149], v[220:223], v[4:7]
	v_mfma_f32_16x16x32_bf16 v[0:3], v[166:169], v[220:223], v[0:3]
	v_mfma_f32_16x16x32_bf16 v[52:55], v[150:153], v[184:187], v[52:55]
	v_mfma_f32_16x16x32_bf16 v[48:51], v[176:179], v[184:187], v[48:51]
	v_mfma_f32_16x16x32_bf16 v[36:39], v[150:153], v[192:195], v[36:39]
	v_mfma_f32_16x16x32_bf16 v[32:35], v[176:179], v[192:195], v[32:35]
	v_mfma_f32_16x16x32_bf16 v[20:23], v[150:153], v[216:219], v[20:23]
	v_mfma_f32_16x16x32_bf16 v[16:19], v[176:179], v[216:219], v[16:19]
	v_mfma_f32_16x16x32_bf16 v[4:7], v[150:153], v[224:227], v[4:7]
	v_mfma_f32_16x16x32_bf16 v[0:3], v[176:179], v[224:227], v[0:3]
	s_setprio 0
	s_barrier
	v_add_u32_e32 v64, s43, v173
	ds_read_b128 v[66:69], v64
	ds_read_b128 v[70:73], v64 offset:1024
	ds_read_b128 v[74:77], v64 offset:2048
	ds_read_b128 v[78:81], v64 offset:3072
	v_add_u32_e32 v64, s48, v173
	ds_read_b128 v[146:149], v64
	ds_read_b128 v[150:153], v64 offset:1024
	ds_read_b128 v[166:169], v64 offset:2048
	ds_read_b128 v[176:179], v64 offset:3072
	s_add_u32 s26, s26, 0x40000
	s_addc_u32 s27, s27, 0
	s_mov_b32 m0, s39
	ds_read_b128 v[180:183], v175 offset:32768
	ds_read_b128 v[184:187], v175 offset:33792
	ds_read_b128 v[188:191], v175 offset:34816
	ds_read_b128 v[192:195], v175 offset:35840
	ds_read_b128 v[212:215], v175 offset:36864
	ds_read_b128 v[216:219], v175 offset:37888
	ds_read_b128 v[220:223], v175 offset:38912
	ds_read_b128 v[224:227], v175 offset:39936
	global_load_lds_dwordx4 v160, s[26:27]
	s_mov_b32 m0, s40
	s_nop 0
	global_load_lds_dwordx4 v156, s[26:27]
	s_waitcnt vmcnt(8)
	s_waitcnt lgkmcnt(0)
	s_barrier
	s_setprio 1
	s_waitcnt lgkmcnt(0)
	v_mfma_f32_16x16x32_bf16 v[142:145], v[66:69], v[180:183], v[142:145]
	v_mfma_f32_16x16x32_bf16 v[138:141], v[74:77], v[180:183], v[138:141]
	v_mfma_f32_16x16x32_bf16 v[126:129], v[66:69], v[188:191], v[126:129]
	v_mfma_f32_16x16x32_bf16 v[122:125], v[74:77], v[188:191], v[122:125]
	v_mfma_f32_16x16x32_bf16 v[110:113], v[66:69], v[212:215], v[110:113]
	v_mfma_f32_16x16x32_bf16 v[106:109], v[74:77], v[212:215], v[106:109]
	v_mfma_f32_16x16x32_bf16 v[94:97], v[66:69], v[220:223], v[94:97]
	v_mfma_f32_16x16x32_bf16 v[90:93], v[74:77], v[220:223], v[90:93]
	v_mfma_f32_16x16x32_bf16 v[142:145], v[70:73], v[184:187], v[142:145]
	v_mfma_f32_16x16x32_bf16 v[138:141], v[78:81], v[184:187], v[138:141]
	v_mfma_f32_16x16x32_bf16 v[126:129], v[70:73], v[192:195], v[126:129]
	v_mfma_f32_16x16x32_bf16 v[122:125], v[78:81], v[192:195], v[122:125]
	v_mfma_f32_16x16x32_bf16 v[110:113], v[70:73], v[216:219], v[110:113]
	v_mfma_f32_16x16x32_bf16 v[106:109], v[78:81], v[216:219], v[106:109]
	v_mfma_f32_16x16x32_bf16 v[94:97], v[70:73], v[224:227], v[94:97]
	v_mfma_f32_16x16x32_bf16 v[90:93], v[78:81], v[224:227], v[90:93]
	s_setprio 0
	s_setprio 1
	v_mfma_f32_16x16x32_bf16 v[134:137], v[146:149], v[180:183], v[134:137]
	v_mfma_f32_16x16x32_bf16 v[130:133], v[166:169], v[180:183], v[130:133]
	v_mfma_f32_16x16x32_bf16 v[118:121], v[146:149], v[188:191], v[118:121]
	v_mfma_f32_16x16x32_bf16 v[114:117], v[166:169], v[188:191], v[114:117]
	v_mfma_f32_16x16x32_bf16 v[102:105], v[146:149], v[212:215], v[102:105]
	v_mfma_f32_16x16x32_bf16 v[98:101], v[166:169], v[212:215], v[98:101]
	v_mfma_f32_16x16x32_bf16 v[86:89], v[146:149], v[220:223], v[86:89]
	v_mfma_f32_16x16x32_bf16 v[82:85], v[166:169], v[220:223], v[82:85]
	v_mfma_f32_16x16x32_bf16 v[134:137], v[150:153], v[184:187], v[134:137]
	v_mfma_f32_16x16x32_bf16 v[130:133], v[176:179], v[184:187], v[130:133]
	v_mfma_f32_16x16x32_bf16 v[118:121], v[150:153], v[192:195], v[118:121]
	v_mfma_f32_16x16x32_bf16 v[114:117], v[176:179], v[192:195], v[114:117]
	v_mfma_f32_16x16x32_bf16 v[102:105], v[150:153], v[216:219], v[102:105]
	v_mfma_f32_16x16x32_bf16 v[98:101], v[176:179], v[216:219], v[98:101]
	v_mfma_f32_16x16x32_bf16 v[86:89], v[150:153], v[224:227], v[86:89]
	v_mfma_f32_16x16x32_bf16 v[82:85], v[176:179], v[224:227], v[82:85]
	s_setprio 0
	s_barrier
	s_mov_b32 m0, s44
	s_add_u32 s100, s4, s68
	s_addc_u32 s101, s5, s69
	s_add_u32 s4, s4, 0x40080
	ds_read_b128 v[180:183], v175 offset:49152
	ds_read_b128 v[184:187], v175 offset:50176
	ds_read_b128 v[188:191], v175 offset:51200
	ds_read_b128 v[192:195], v175 offset:52224
	ds_read_b128 v[212:215], v175 offset:53248
	ds_read_b128 v[216:219], v175 offset:54272
	ds_read_b128 v[220:223], v175 offset:55296
	ds_read_b128 v[224:227], v175 offset:56320
	global_load_lds_dwordx4 v158, s[100:101]
	s_mov_b32 m0, s45
	s_addc_u32 s5, s5, 0
	global_load_lds_dwordx4 v154, s[100:101]
	s_mov_b32 m0, s49
	s_add_u32 s100, s26, s68
	global_load_lds_dwordx4 v158, s[4:5]
	s_addc_u32 s101, s27, s69
	s_mov_b32 m0, s50
	s_sub_u32 s100, s100, 0x40000
	global_load_lds_dwordx4 v154, s[4:5]
	s_subb_u32 s101, s101, 0
	s_mov_b32 m0, s46
	s_nop 0
	global_load_lds_dwordx4 v160, s[100:101]
	s_mov_b32 m0, s47
	s_nop 0
	global_load_lds_dwordx4 v156, s[100:101]
	s_waitcnt vmcnt(8)
	s_waitcnt lgkmcnt(0)
	s_barrier
	s_setprio 1
	s_waitcnt lgkmcnt(0)
	v_mfma_f32_16x16x32_bf16 v[60:63], v[66:69], v[180:183], v[60:63]
	v_mfma_f32_16x16x32_bf16 v[56:59], v[74:77], v[180:183], v[56:59]
	v_mfma_f32_16x16x32_bf16 v[44:47], v[66:69], v[188:191], v[44:47]
	v_mfma_f32_16x16x32_bf16 v[40:43], v[74:77], v[188:191], v[40:43]
	v_mfma_f32_16x16x32_bf16 v[28:31], v[66:69], v[212:215], v[28:31]
	v_mfma_f32_16x16x32_bf16 v[24:27], v[74:77], v[212:215], v[24:27]
	v_mfma_f32_16x16x32_bf16 v[12:15], v[66:69], v[220:223], v[12:15]
	v_mfma_f32_16x16x32_bf16 v[8:11], v[74:77], v[220:223], v[8:11]
	v_mfma_f32_16x16x32_bf16 v[60:63], v[70:73], v[184:187], v[60:63]
	v_mfma_f32_16x16x32_bf16 v[56:59], v[78:81], v[184:187], v[56:59]
	v_mfma_f32_16x16x32_bf16 v[44:47], v[70:73], v[192:195], v[44:47]
	v_mfma_f32_16x16x32_bf16 v[40:43], v[78:81], v[192:195], v[40:43]
	v_mfma_f32_16x16x32_bf16 v[28:31], v[70:73], v[216:219], v[28:31]
	v_mfma_f32_16x16x32_bf16 v[24:27], v[78:81], v[216:219], v[24:27]
	v_mfma_f32_16x16x32_bf16 v[12:15], v[70:73], v[224:227], v[12:15]
	v_mfma_f32_16x16x32_bf16 v[8:11], v[78:81], v[224:227], v[8:11]
	s_setprio 0
	s_setprio 1
	v_mfma_f32_16x16x32_bf16 v[52:55], v[146:149], v[180:183], v[52:55]
	v_mfma_f32_16x16x32_bf16 v[48:51], v[166:169], v[180:183], v[48:51]
	v_mfma_f32_16x16x32_bf16 v[36:39], v[146:149], v[188:191], v[36:39]
	v_mfma_f32_16x16x32_bf16 v[32:35], v[166:169], v[188:191], v[32:35]
	v_mfma_f32_16x16x32_bf16 v[20:23], v[146:149], v[212:215], v[20:23]
	v_mfma_f32_16x16x32_bf16 v[16:19], v[166:169], v[212:215], v[16:19]
	v_mfma_f32_16x16x32_bf16 v[4:7], v[146:149], v[220:223], v[4:7]
	v_mfma_f32_16x16x32_bf16 v[0:3], v[166:169], v[220:223], v[0:3]
	v_mfma_f32_16x16x32_bf16 v[52:55], v[150:153], v[184:187], v[52:55]
	v_mfma_f32_16x16x32_bf16 v[48:51], v[176:179], v[184:187], v[48:51]
	v_mfma_f32_16x16x32_bf16 v[36:39], v[150:153], v[192:195], v[36:39]
	v_mfma_f32_16x16x32_bf16 v[32:35], v[176:179], v[192:195], v[32:35]
	v_mfma_f32_16x16x32_bf16 v[20:23], v[150:153], v[216:219], v[20:23]
	v_mfma_f32_16x16x32_bf16 v[16:19], v[176:179], v[216:219], v[16:19]
	v_mfma_f32_16x16x32_bf16 v[4:7], v[150:153], v[224:227], v[4:7]
	v_mfma_f32_16x16x32_bf16 v[0:3], v[176:179], v[224:227], v[0:3]
	s_add_i32 s61, s61, 2
	s_add_u32 s0, s0, 0x100
	s_addc_u32 s1, s1, 0
	s_add_u32 s59, s59, 0x100
	s_addc_u32 s60, s60, 0
	s_cmp_gt_u32 s61, 13
	s_setprio 0
	s_barrier
	s_cbranch_scc0 .LBB0_814
	s_and_b64 vcc, exec, s[20:21]
	s_cbranch_vccz .LBB0_817
	s_barrier
